# v78: gdn_gb step body list-scheduled (VALU/LDS spread under the MFMAs, decay factor read early, wide transposed output stores, last 4 state MFMAs rotated to next step top)
# speedup vs baseline: 1.0071x; 1.0071x over previous
.LBB0_1631:
	s_andn2_b64 vcc, exec, s[0:1]
	s_cbranch_vccnz .LBB0_1638
	s_waitcnt vmcnt(0)
	v_and_b32_e32 v4, 31, v2
	v_lshrrev_b32_e32 v2, 2, v2
	v_and_b32_e32 v2, 8, v2
	v_sub_u32_e32 v5, v4, v2
	v_cmp_eq_u32_e32 vcc, 1, v5
	v_mov_b32_e32 v7, 0x3f80
	s_lshl_b32 s0, s8, 5
	v_cndmask_b32_e64 v6, 0, 1.0, vcc
	v_cmp_ne_u32_e32 vcc, v4, v2
	v_or_b32_e32 v2, 16, v2
	s_add_i32 s0, s0, s2
	v_cndmask_b32_e32 v132, v7, v6, vcc
	v_cmp_eq_u32_e32 vcc, 3, v5
	s_lshl_b32 s25, s38, 6
	s_barrier
	s_cmp_eq_u32 s39, 0
	v_cndmask_b32_e64 v6, 0, 1.0, vcc
	v_cmp_ne_u32_e32 vcc, 2, v5
	s_cselect_b64 s[8:9], -1, 0
	s_lshl_b32 s40, s38, 2
	v_cndmask_b32_e32 v133, v7, v6, vcc
	v_cmp_eq_u32_e32 vcc, 5, v5
	s_lshl_b32 s10, s3, 1
	s_bitset1_b32 s40, 8
	v_cndmask_b32_e64 v6, 0, 1.0, vcc
	v_cmp_ne_u32_e32 vcc, 4, v5
	s_andn2_b32 s41, s41, 63
	s_ashr_i32 s1, s0, 31
	v_cndmask_b32_e32 v134, v7, v6, vcc
	v_cmp_eq_u32_e32 vcc, 7, v5
	s_or_b32 s42, s10, s39
	s_movk_i32 s43, 0x43
	v_cndmask_b32_e64 v6, 0, 1.0, vcc
	v_cmp_ne_u32_e32 vcc, 6, v5
	v_sub_u32_e32 v5, v4, v2
	s_mov_b32 s46, -4
	v_cndmask_b32_e32 v135, v7, v6, vcc
	v_cmp_eq_u32_e32 vcc, 1, v5
	s_nop 1
	v_cndmask_b32_e64 v6, 0, 1.0, vcc
	v_cmp_ne_u32_e32 vcc, v4, v2
	v_mov_b32_e32 v4, 0
	v_mov_b32_e32 v8, v4
	v_cndmask_b32_e32 v136, v7, v6, vcc
	v_cmp_eq_u32_e32 vcc, 3, v5
	v_mov_b32_e32 v6, v4
	v_mov_b32_e32 v9, v4
	v_cndmask_b32_e64 v2, 0, 1.0, vcc
	v_cmp_ne_u32_e32 vcc, 2, v5
	v_mov_b32_e32 v10, v4
	v_mov_b32_e32 v11, v4
	v_cndmask_b32_e32 v137, v7, v2, vcc
	v_cmp_eq_u32_e32 vcc, 5, v5
	v_mov_b32_e32 v12, v4
	v_mov_b32_e32 v13, v4
	v_cndmask_b32_e64 v2, 0, 1.0, vcc
	v_cmp_ne_u32_e32 vcc, 4, v5
	v_mov_b32_e32 v14, v4
	v_mov_b32_e32 v15, v4
	v_cndmask_b32_e32 v138, v7, v2, vcc
	v_cmp_eq_u32_e32 vcc, 7, v5
	v_mov_b32_e32 v16, v4
	v_mov_b32_e32 v17, v4
	v_cndmask_b32_e64 v2, 0, 1.0, vcc
	v_cmp_ne_u32_e32 vcc, 6, v5
	v_mov_b32_e32 v5, v4
	v_mov_b32_e32 v18, v4
	v_cndmask_b32_e32 v139, v7, v2, vcc
	v_mov_b32_e32 v7, v4
	v_mov_b32_e32 v19, v4
	v_mov_b32_e32 v20, v4
	v_mov_b32_e32 v21, v4
	v_mov_b32_e32 v22, v4
	v_mov_b32_e32 v23, v4
	v_mov_b32_e32 v24, v4
	v_mov_b32_e32 v25, v4
	v_mov_b32_e32 v26, v4
	v_mov_b32_e32 v27, v4
	v_mov_b32_e32 v28, v4
	v_mov_b32_e32 v29, v4
	v_mov_b32_e32 v30, v4
	v_mov_b32_e32 v31, v4
	v_mov_b32_e32 v32, v4
	v_mov_b32_e32 v33, v4
	v_mov_b32_e32 v34, v4
	v_mov_b32_e32 v35, v4
	s_waitcnt vmcnt(0)
	v_mov_b32_e32 v36, v4
	v_mov_b32_e32 v37, v4
	v_mov_b32_e32 v38, v4
	v_mov_b32_e32 v39, v4
	v_mov_b32_e32 v40, v4
	v_mov_b32_e32 v41, v4
	v_mov_b32_e32 v42, v4
	v_mov_b32_e32 v43, v4
	v_mov_b32_e32 v44, v4
	v_mov_b32_e32 v45, v4
	v_mov_b32_e32 v46, v4
	v_mov_b32_e32 v47, v4
	v_mov_b32_e32 v48, v4
	v_mov_b32_e32 v49, v4
	v_mov_b32_e32 v50, v4
	v_mov_b32_e32 v51, v4
	v_mov_b32_e32 v52, v4
	v_mov_b32_e32 v53, v4
	v_mov_b32_e32 v54, v4
	v_mov_b32_e32 v55, v4
	v_mov_b32_e32 v56, v4
	v_mov_b32_e32 v57, v4
	v_mov_b32_e32 v58, v4
	v_mov_b32_e32 v59, v4
	v_mov_b32_e32 v60, v4
	v_mov_b32_e32 v61, v4
	v_mov_b32_e32 v62, v4
	v_mov_b32_e32 v63, v4
	v_mov_b32_e32 v64, v4
	v_mov_b32_e32 v65, v4
	v_mov_b32_e32 v66, v4
	v_mov_b32_e32 v67, v4
	v_mov_b32_e32 v100, v4
	v_mov_b32_e32 v101, v4
	v_mov_b32_e32 v102, v4
	v_mov_b32_e32 v103, v4
	v_mov_b32_e32 v164, v4
	v_mov_b32_e32 v165, v4
	v_mov_b32_e32 v166, v4
	v_mov_b32_e32 v167, v4
	v_mov_b32_e32 v178, v4
	v_mov_b32_e32 v179, v4
	v_mov_b32_e32 v180, v4
	v_mov_b32_e32 v181, v4
	v_mov_b32_e32 v190, v4
	v_mov_b32_e32 v191, v4
	v_mov_b32_e32 v192, v4
	v_mov_b32_e32 v193, v4
	v_mov_b32_e32 v194, v4
	v_mov_b32_e32 v195, v4
	v_mov_b32_e32 v196, v4
	v_mov_b32_e32 v197, v4
	s_branch .LBB0_1634
.LBB0_1633:
	v_mfma_f32_32x32x16_bf16 v[52:67], v[164:167], v[100:103], v[52:67]
	s_lshl_b32 s10, s50, 4
	s_bitcmp1_b32 s47, 0
	v_and_b32_e32 v2, 31, v68
	v_ashrrev_i32_e32 v177, 5, v68
	v_mul_u32_u24_e32 v68, 0x110, v2
	v_lshlrev_b32_e32 v168, 3, v177
	v_mfma_f32_32x32x16_bf16 v[36:51], v[178:181], v[100:103], v[36:51]
	s_cselect_b32 s11, 0x11c00, 0
	v_add_u32_e32 v178, s11, v1
	ds_read_b32 v234, v178 offset:62976
	v_add3_u32 v169, v178, v68, v168
	v_add_u32_e32 v237, 0x2000, v169
	ds_read2_b64 v[88:91], v237 offset0:64 offset1:66
	v_mfma_f32_32x32x16_bf16 v[20:35], v[190:193], v[100:103], v[20:35]
	ds_read2_b64 v[92:95], v237 offset0:68 offset1:70
	ds_read2_b64 v[96:99], v237 offset0:72 offset1:74
	ds_read2_b64 v[116:119], v237 offset0:76 offset1:78
	ds_read2_b64 v[68:71], v169 offset1:2
	s_nop 0
	v_cvt_pk_bf16_f32 v160, v36, v37
	v_cvt_pk_bf16_f32 v161, v38, v39
	v_mfma_f32_32x32x16_bf16 v[4:19], v[194:197], v[100:103], v[4:19]
	v_cvt_pk_bf16_f32 v162, v40, v41
	v_cvt_pk_bf16_f32 v163, v42, v43
	v_cvt_pk_bf16_f32 v164, v44, v45
	v_cvt_pk_bf16_f32 v165, v46, v47
	v_cvt_pk_bf16_f32 v166, v48, v49
	v_cvt_pk_bf16_f32 v167, v50, v51
	v_cvt_pk_bf16_f32 v84, v52, v53
	v_cvt_pk_bf16_f32 v85, v54, v55
	v_cvt_pk_bf16_f32 v86, v56, v57
	v_cvt_pk_bf16_f32 v87, v58, v59
	s_waitcnt lgkmcnt(4)
	s_nop 0
	v_mfma_f32_32x32x16_bf16 v[100:115], v[88:91], v[84:87], 0
	ds_read2_b64 v[72:75], v169 offset0:4 offset1:6
	ds_read2_b64 v[76:79], v169 offset0:8 offset1:10
	ds_read2_b64 v[80:83], v169 offset0:12 offset1:14
	ds_read2_b64 v[184:187], v237 offset0:80 offset1:82
	v_cvt_pk_bf16_f32 v156, v60, v61
	v_cvt_pk_bf16_f32 v157, v62, v63
	v_cvt_pk_bf16_f32 v158, v64, v65
	v_cvt_pk_bf16_f32 v159, v66, v67
	s_waitcnt lgkmcnt(7)
	s_nop 0
	v_mfma_f32_32x32x16_bf16 v[100:115], v[92:95], v[156:159], v[100:115]
	v_cvt_pk_bf16_f32 v144, v20, v21
	v_cvt_pk_bf16_f32 v145, v22, v23
	v_cvt_pk_bf16_f32 v146, v24, v25
	v_cvt_pk_bf16_f32 v147, v26, v27
	ds_read2_b64 v[188:191], v237 offset0:84 offset1:86
	v_cvt_pk_bf16_f32 v152, v28, v29
	s_waitcnt lgkmcnt(7)
	v_mfma_f32_32x32x16_bf16 v[100:115], v[96:99], v[160:163], v[100:115]
	v_cvt_pk_bf16_f32 v153, v30, v31
	v_cvt_pk_bf16_f32 v154, v32, v33
	v_cvt_pk_bf16_f32 v155, v34, v35
	ds_read2_b64 v[196:199], v237 offset0:88 offset1:90
	v_cvt_pk_bf16_f32 v148, v4, v5
	v_cvt_pk_bf16_f32 v149, v6, v7
	s_waitcnt lgkmcnt(7)
	v_mfma_f32_32x32x16_bf16 v[100:115], v[116:119], v[164:167], v[100:115]
	v_cvt_pk_bf16_f32 v150, v8, v9
	v_cvt_pk_bf16_f32 v151, v10, v11
	ds_read2_b64 v[204:207], v237 offset0:92 offset1:94
	v_cvt_pk_bf16_f32 v140, v12, v13
	v_cvt_pk_bf16_f32 v141, v14, v15
	v_cvt_pk_bf16_f32 v142, v16, v17
	s_waitcnt lgkmcnt(7)
	v_mfma_f32_32x32x16_bf16 v[116:131], v[68:71], v[84:87], 0
	v_cvt_pk_bf16_f32 v143, v18, v19
	ds_read2_b64 v[170:173], v169 offset0:16 offset1:18
	ds_read2_b64 v[180:183], v169 offset0:20 offset1:22
	ds_read2_b64 v[192:195], v169 offset0:24 offset1:26
	ds_read2_b64 v[200:203], v169 offset0:28 offset1:30
	v_add_u32_e32 v239, 0x6000, v169
	s_waitcnt lgkmcnt(10)
	v_mfma_f32_32x32x16_bf16 v[116:131], v[72:75], v[156:159], v[116:131]
	ds_read2_b64 v[68:71], v239 offset0:192 offset1:194
	ds_read2_b64 v[92:95], v239 offset0:196 offset1:198
	ds_read2_b64 v[96:99], v239 offset0:200 offset1:202
	ds_read2_b64 v[220:223], v239 offset0:204 offset1:206
	v_add_u32_e32 v238, 0x4000, v169
	ds_read2_b64 v[88:91], v238 offset0:128 offset1:130
	s_waitcnt lgkmcnt(14)
	v_mfma_f32_32x32x16_bf16 v[116:131], v[76:79], v[160:163], v[116:131]
	ds_read2_b64 v[208:211], v238 offset0:132 offset1:134
	ds_read2_b64 v[212:215], v238 offset0:136 offset1:138
	ds_read2_b64 v[216:219], v238 offset0:140 offset1:142
	ds_read2_b64 v[224:227], v239 offset0:220 offset1:222
	v_mul_f32_e64 v66, v66, v234
	v_mul_f32_e64 v67, v67, v234
	s_waitcnt lgkmcnt(15)
	v_mfma_f32_32x32x16_bf16 v[116:131], v[80:83], v[164:167], v[116:131]
	v_mul_f32_e64 v64, v64, v234
	v_mul_f32_e64 v65, v65, v234
	v_mul_f32_e64 v62, v62, v234
	v_mul_f32_e64 v63, v63, v234
	v_mul_f32_e64 v60, v60, v234
	v_mul_f32_e64 v61, v61, v234
	v_mfma_f32_32x32x16_bf16 v[100:115], v[184:187], v[144:147], v[100:115]
	ds_read2_b64 v[184:187], v239 offset0:208 offset1:210
	v_mul_f32_e64 v58, v58, v234
	v_mul_f32_e64 v59, v59, v234
	v_mul_f32_e64 v56, v56, v234
	v_mul_f32_e64 v57, v57, v234
	v_mul_f32_e64 v54, v54, v234
	v_mfma_f32_32x32x16_bf16 v[100:115], v[188:191], v[152:155], v[100:115]
	ds_read2_b64 v[188:191], v239 offset0:212 offset1:214
	v_mul_f32_e64 v55, v55, v234
	v_mul_f32_e64 v52, v52, v234
	v_mul_f32_e64 v53, v53, v234
	v_mul_f32_e64 v50, v50, v234
	v_mul_f32_e64 v51, v51, v234
	s_waitcnt lgkmcnt(15)
	v_mfma_f32_32x32x16_bf16 v[100:115], v[196:199], v[148:151], v[100:115]
	ds_read2_b64 v[196:199], v239 offset0:216 offset1:218
	v_mul_f32_e64 v48, v48, v234
	v_mul_f32_e64 v49, v49, v234
	v_mul_f32_e64 v46, v46, v234
	v_mul_f32_e64 v47, v47, v234
	v_mul_f32_e64 v44, v44, v234
	v_mfma_f32_32x32x16_bf16 v[100:115], v[204:207], v[140:143], v[100:115]
	ds_read2_b64 v[204:207], v238 offset0:156 offset1:158
	v_mul_f32_e64 v45, v45, v234
	v_mul_f32_e64 v42, v42, v234
	v_mul_f32_e64 v43, v43, v234
	v_mul_f32_e64 v40, v40, v234
	v_mul_f32_e64 v41, v41, v234
	s_waitcnt lgkmcnt(15)
	v_mfma_f32_32x32x16_bf16 v[116:131], v[170:173], v[144:147], v[116:131]
	ds_read2_b64 v[170:173], v238 offset0:144 offset1:146
	v_mul_f32_e64 v38, v38, v234
	v_mul_f32_e64 v39, v39, v234
	v_mul_f32_e64 v36, v36, v234
	v_mul_f32_e64 v37, v37, v234
	v_mul_f32_e64 v34, v34, v234
	v_mfma_f32_32x32x16_bf16 v[116:131], v[180:183], v[152:155], v[116:131]
	ds_read2_b64 v[180:183], v238 offset0:148 offset1:150
	v_mul_f32_e64 v35, v35, v234
	v_mul_f32_e64 v32, v32, v234
	v_mul_f32_e64 v33, v33, v234
	v_mul_f32_e64 v30, v30, v234
	v_mul_f32_e64 v31, v31, v234
	s_waitcnt lgkmcnt(15)
	v_mfma_f32_32x32x16_bf16 v[116:131], v[192:195], v[148:151], v[116:131]
	ds_read2_b64 v[192:195], v238 offset0:152 offset1:154
	v_mul_f32_e64 v28, v28, v234
	v_mul_f32_e64 v29, v29, v234
	v_mul_f32_e64 v26, v26, v234
	v_mul_f32_e64 v27, v27, v234
	v_mul_f32_e64 v24, v24, v234
	v_mfma_f32_32x32x16_bf16 v[116:131], v[200:203], v[140:143], v[116:131]
	v_mul_f32_e64 v25, v25, v234
	v_mul_f32_e64 v22, v22, v234
	v_mul_f32_e64 v23, v23, v234
	v_mul_f32_e64 v20, v20, v234
	v_mul_f32_e64 v21, v21, v234
	v_mul_f32_e64 v18, v18, v234
	s_waitcnt lgkmcnt(15)
	v_mfma_f32_32x32x16_bf16 v[68:83], v[84:87], v[68:71], 0
	v_mul_f32_e64 v19, v19, v234
	v_mul_f32_e64 v16, v16, v234
	v_mul_f32_e64 v17, v17, v234
	v_mul_f32_e64 v14, v14, v234
	v_mul_f32_e64 v15, v15, v234
	v_mul_f32_e64 v12, v12, v234
	s_waitcnt lgkmcnt(14)
	v_mfma_f32_32x32x16_bf16 v[68:83], v[156:159], v[92:95], v[68:83]
	v_mul_f32_e64 v13, v13, v234
	v_mul_f32_e64 v10, v10, v234
	v_mul_f32_e64 v11, v11, v234
	v_mul_f32_e64 v8, v8, v234
	v_mul_f32_e64 v9, v9, v234
	v_mul_f32_e64 v6, v6, v234
	s_waitcnt lgkmcnt(13)
	v_mfma_f32_32x32x16_bf16 v[68:83], v[160:163], v[96:99], v[68:83]
	v_mul_f32_e64 v7, v7, v234
	v_mul_f32_e64 v4, v4, v234
	v_mul_f32_e64 v5, v5, v234
	s_or_b32 s10, s10, s42
	s_ashr_i32 s11, s10, 31
	s_lshl_b64 s[10:11], s[10:11], 14
	s_waitcnt lgkmcnt(12)
	v_mfma_f32_32x32x16_bf16 v[68:83], v[164:167], v[220:223], v[68:83]
	s_add_u32 s10, s26, s10
	s_addc_u32 s11, s27, s11
	s_add_u32 s10, s10, s0
	s_addc_u32 s11, s11, s1
	s_add_u32 s10, s10, s0
	s_addc_u32 s11, s11, s1
	s_waitcnt lgkmcnt(11)
	v_mfma_f32_32x32x16_bf16 v[84:99], v[84:87], v[88:91], 0
	v_lshlrev_b32_e32 v235, 4, v177
	v_lshl_add_u32 v235, v2, 8, v235
	v_add_u32_e32 v236, 0x2000, v235
	s_waitcnt lgkmcnt(10)
	v_mfma_f32_32x32x16_bf16 v[84:99], v[156:159], v[208:211], v[84:99]
	v_lshlrev_b32_e32 v156, 4, v177
	v_add3_u32 v156, v178, s41, v156
	v_mad_u32_u24 v158, v2, s33, v156
	ds_read_b128 v[200:203], v158 offset:63488
	ds_read_b128 v[208:211], v158 offset:63520
	v_mov_b32_e32 v159, 0x1200
	s_waitcnt lgkmcnt(11)
	v_mfma_f32_32x32x16_bf16 v[84:99], v[160:163], v[212:215], v[84:99]
	v_mad_u32_u24 v159, v2, s33, v159
	v_add_u32_e32 v156, v156, v159
	ds_read_b128 v[212:215], v156 offset:63488
	ds_read_b128 v[220:223], v156 offset:63520
	v_add3_u32 v232, v178, v159, v168
	v_mul_u32_u24_e32 v157, 0x90, v2
	s_waitcnt lgkmcnt(12)
	v_mfma_f32_32x32x16_bf16 v[84:99], v[164:167], v[216:219], v[84:99]
	v_add3_u32 v179, v178, v157, v168
	v_add_u32_e32 v156, 0xd000, v179
	ds_read2_b64 v[216:219], v156 offset0:4 offset1:6
	ds_read2_b64 v[228:231], v156 offset0:12 offset1:14
	v_add_u32_e32 v157, 0xd000, v232
	ds_read2_b64 v[164:167], v157 offset0:4 offset1:6
	s_waitcnt lgkmcnt(9)
	v_mfma_f32_32x32x16_bf16 v[84:99], v[144:147], v[170:173], v[84:99]
	ds_read2_b64 v[168:171], v157 offset1:2
	ds_read2_b64 v[160:163], v157 offset0:8 offset1:10
	s_waitcnt lgkmcnt(10)
	v_mfma_f32_32x32x16_bf16 v[84:99], v[152:155], v[180:183], v[84:99]
	ds_read2_b64 v[180:183], v156 offset1:2
	s_waitcnt lgkmcnt(10)
	v_mfma_f32_32x32x16_bf16 v[84:99], v[148:151], v[192:195], v[84:99]
	ds_read2_b64 v[192:195], v156 offset0:8 offset1:10
	ds_read2_b64 v[156:159], v157 offset0:12 offset1:14
	v_mfma_f32_32x32x16_bf16 v[84:99], v[140:143], v[204:207], v[84:99]
	s_waitcnt lgkmcnt(11)
	v_mfma_f32_32x32x16_bf16 v[116:131], v[200:203], v[132:135], v[116:131]
	s_waitcnt lgkmcnt(9)
	v_mfma_f32_32x32x16_bf16 v[100:115], v[212:215], v[132:135], v[100:115]
	v_mfma_f32_32x32x16_bf16 v[116:131], v[208:211], v[136:139], v[116:131]
	s_waitcnt lgkmcnt(8)
	v_mfma_f32_32x32x16_bf16 v[100:115], v[220:223], v[136:139], v[100:115]
	v_mfma_f32_32x32x16_bf16 v[68:83], v[144:147], v[184:187], v[68:83]
	v_add_u32_e32 v184, 0x8800, v179
	v_add_u32_e32 v185, 0x8800, v232
	v_mfma_f32_32x32x16_bf16 v[68:83], v[152:155], v[188:191], v[68:83]
	v_add_u32_e32 v190, 0xa800, v179
	v_mfma_f32_32x32x16_bf16 v[68:83], v[148:151], v[196:199], v[68:83]
	v_add_u32_e32 v196, 0xb800, v179
	ds_read2_b64 v[144:147], v196 offset0:192 offset1:194
	ds_read2_b64 v[148:151], v190 offset0:132 offset1:134
	ds_read2_b64 v[152:155], v196 offset0:196 offset1:198
	v_cvt_pk_bf16_f32 v172, v116, v117
	v_cvt_pk_bf16_f32 v173, v118, v119
	v_mfma_f32_32x32x16_bf16 v[68:83], v[140:143], v[224:227], v[68:83]
	v_cvt_pk_bf16_f32 v118, v104, v105
	v_cvt_pk_bf16_f32 v119, v106, v107
	v_cvt_pk_bf16_f32 v174, v120, v121
	v_cvt_pk_bf16_f32 v120, v124, v125
	v_cvt_pk_bf16_f32 v121, v126, v127
	v_cvt_pk_bf16_f32 v175, v122, v123
	s_waitcnt lgkmcnt(5)
	s_nop 0
	v_mfma_f32_32x32x16_bf16 v[84:99], v[172:175], v[180:183], v[84:99]
	v_cvt_pk_bf16_f32 v122, v128, v129
	v_cvt_pk_bf16_f32 v123, v130, v131
	ds_read2_b64 v[124:127], v185 offset1:2
	v_cvt_pk_bf16_f32 v116, v100, v101
	v_cvt_pk_bf16_f32 v100, v108, v109
	v_cvt_pk_bf16_f32 v101, v110, v111
	v_mfma_f32_32x32x16_bf16 v[84:99], v[120:123], v[216:219], v[84:99]
	ds_read2_b64 v[108:111], v184 offset1:2
	v_cvt_pk_bf16_f32 v117, v102, v103
	v_cvt_pk_bf16_f32 v102, v112, v113
	v_cvt_pk_bf16_f32 v103, v114, v115
	ds_read2_b64 v[128:131], v190 offset0:128 offset1:130
	ds_read2_b64 v[104:107], v184 offset0:4 offset1:6
	s_waitcnt lgkmcnt(8)
	v_mfma_f32_32x32x16_bf16 v[84:99], v[116:119], v[192:195], v[84:99]
	ds_read2_b64 v[112:115], v185 offset0:4 offset1:6
	ds_read2_b64 v[140:143], v184 offset0:8 offset1:10
	ds_read2_b64 v[178:181], v185 offset0:12 offset1:14
	ds_read2_b64 v[186:189], v196 offset0:200 offset1:202
	ds_read2_b64 v[194:197], v196 offset0:204 offset1:206
	v_mfma_f32_32x32x16_bf16 v[84:99], v[100:103], v[228:231], v[84:99]
	v_mfma_f32_32x32x16_bf16 v[68:83], v[172:175], v[168:171], v[68:83]
	ds_read2_b64 v[168:171], v185 offset0:8 offset1:10
	v_mfma_f32_32x32x16_bf16 v[68:83], v[120:123], v[164:167], v[68:83]
	ds_read2_b64 v[164:167], v184 offset0:12 offset1:14
	ds_read2_b64 v[182:185], v190 offset0:136 offset1:138
	ds_read2_b64 v[190:193], v190 offset0:140 offset1:142
	v_mfma_f32_32x32x16_bf16 v[68:83], v[116:119], v[160:163], v[68:83]
	s_waitcnt lgkmcnt(15)
	v_mfma_f32_32x32x16_bf16 v[68:83], v[100:103], v[156:159], v[68:83]
	s_waitcnt lgkmcnt(11)
	v_mfma_f32_32x32x16_bf16 v[52:67], v[108:111], v[172:175], v[52:67]
	v_mfma_f32_32x32x16_bf16 v[36:51], v[124:127], v[172:175], v[36:51]
	s_waitcnt lgkmcnt(10)
	v_mfma_f32_32x32x16_bf16 v[20:35], v[128:131], v[172:175], v[20:35]
	v_cvt_pk_bf16_f32 v84, v84, v85
	v_cvt_pk_bf16_f32 v85, v86, v87
	v_cvt_pk_bf16_f32 v86, v88, v89
	v_cvt_pk_bf16_f32 v87, v90, v91
	v_cvt_pk_bf16_f32 v88, v92, v93
	v_cvt_pk_bf16_f32 v89, v94, v95
	v_mfma_f32_32x32x16_bf16 v[4:19], v[144:147], v[172:175], v[4:19]
	v_cvt_pk_bf16_f32 v90, v96, v97
	v_cvt_pk_bf16_f32 v91, v98, v99
	v_permlane32_swap_b32_e32 v84, v86
	v_permlane32_swap_b32_e32 v85, v87
	v_permlane32_swap_b32_e32 v88, v90
	v_permlane32_swap_b32_e32 v89, v91
	s_waitcnt lgkmcnt(9)
	v_mfma_f32_32x32x16_bf16 v[52:67], v[104:107], v[120:123], v[52:67]
	global_store_dwordx4 v235, v[84:87], s[10:11]
	global_store_dwordx4 v235, v[88:91], s[10:11] offset:32
	v_cvt_pk_bf16_f32 v68, v68, v69
	v_cvt_pk_bf16_f32 v69, v70, v71
	v_cvt_pk_bf16_f32 v70, v72, v73
	v_cvt_pk_bf16_f32 v71, v74, v75
	s_waitcnt lgkmcnt(8)
	v_mfma_f32_32x32x16_bf16 v[36:51], v[112:115], v[120:123], v[36:51]
	v_cvt_pk_bf16_f32 v72, v76, v77
	v_cvt_pk_bf16_f32 v73, v78, v79
	v_cvt_pk_bf16_f32 v74, v80, v81
	v_cvt_pk_bf16_f32 v75, v82, v83
	v_permlane32_swap_b32_e32 v68, v70
	v_permlane32_swap_b32_e32 v69, v71
	v_mfma_f32_32x32x16_bf16 v[20:35], v[148:151], v[120:123], v[20:35]
	v_permlane32_swap_b32_e32 v72, v74
	v_permlane32_swap_b32_e32 v73, v75
	global_store_dwordx4 v236, v[68:71], s[10:11]
	global_store_dwordx4 v236, v[72:75], s[10:11] offset:32
	v_mfma_f32_32x32x16_bf16 v[4:19], v[152:155], v[120:123], v[4:19]
	s_waitcnt lgkmcnt(7)
	v_mfma_f32_32x32x16_bf16 v[52:67], v[140:143], v[116:119], v[52:67]
	s_waitcnt lgkmcnt(3)
	v_mfma_f32_32x32x16_bf16 v[36:51], v[168:171], v[116:119], v[36:51]
	s_waitcnt lgkmcnt(1)
	v_mfma_f32_32x32x16_bf16 v[20:35], v[182:185], v[116:119], v[20:35]
	v_mfma_f32_32x32x16_bf16 v[4:19], v[186:189], v[116:119], v[4:19]
	s_waitcnt lgkmcnt(0)
	s_barrier
	s_add_i32 s43, s43, -1
	s_add_i32 s46, s46, 1
	s_cmp_lg_u32 s43, -1
	s_cbranch_scc0 .LBB0_1638
